# v048 + P6/P16: next-unit gather index loads no longer waited at the unit top, and the first K iteration of each unit waits with vmcnt(10)/(16) so the epilogue store acks drain under the first two phas
# baseline (speedup 1.0000x reference)
.LBB0_495:
	s_lshl_b32 s6, s6, 5
	s_and_b32 s12, s6, 0x60
	s_lshl_b32 s1, s3, 13
	s_lshl_b32 s14, s12, 7
	s_add_u32 s46, s70, 0x605000
	s_addc_u32 s47, s71, 0
	s_add_i32 s48, s27, 0x18000
	s_mov_b64 s[6:7], 0x80
	s_add_i32 s49, s27, 0x1a000
	v_lshl_add_u64 v[4:5], v[4:5], 0, s[6:7]
	s_mov_b32 m0, s48
	s_add_u32 s8, s70, 0x19200080
	s_waitcnt vmcnt(2)
	s_barrier
	global_load_lds_dwordx4 v[4:5], off
	v_lshl_add_u64 v[2:3], v[2:3], 0, s[6:7]
	s_mov_b32 m0, s49
	s_addc_u32 s9, s71, 0
	s_add_i32 s50, s27, 0x8000
	s_add_i32 s51, s27, 0xa000
	global_load_lds_dwordx4 v[2:3], off
	v_lshl_add_u64 v[2:3], s[8:9], 0, v[166:167]
	s_mov_b32 m0, s50
	s_add_u32 s10, s18, 0x20080
	global_load_lds_dwordx4 v[2:3], off
	v_lshl_add_u64 v[2:3], s[8:9], 0, v[168:169]
	s_mov_b32 m0, s51
	s_addc_u32 s11, s19, 0
	s_add_i32 s52, s27, 0x1c000
	global_load_lds_dwordx4 v[2:3], off
	v_lshl_add_u64 v[2:3], s[10:11], 0, v[162:163]
	s_mov_b32 m0, s52
	s_add_i32 s53, s27, 0x1e000
	global_load_lds_dwordx4 v[2:3], off
	v_lshl_add_u64 v[2:3], s[10:11], 0, v[164:165]
	s_mov_b32 m0, s53
	v_lshlrev_b32_e32 v5, 6, v0
	global_load_lds_dwordx4 v[2:3], off
	v_and_b32_e32 v2, 15, v0
	v_bfe_u32 v3, v0, 4, 2
	v_lshl_or_b32 v189, s3, 6, v2
	v_lshlrev_b32_e32 v4, 4, v3
	s_movk_i32 s3, 0x3c0
	v_lshlrev_b32_e32 v6, 2, v0
	v_lshl_or_b32 v2, v2, 6, v4
	v_and_or_b32 v5, v5, s3, v4
	v_and_b32_e32 v6, 32, v6
	s_waitcnt vmcnt(0)
	s_add_i32 s3, s14, 0
	v_xad_u32 v5, v5, v6, s3
	v_xad_u32 v2, v2, v6, 0
	s_cmpk_lt_u32 s2, 0x100
	v_lshl_or_b32 v170, v3, 3, s12
	v_bfe_u32 v3, v0, 4, 1
	s_cselect_b64 s[10:11], -1, 0
	v_lshlrev_b32_e32 v190, 3, v3
	v_lshlrev_b32_e32 v191, 4, v3
	v_or_b32_e32 v192, 32, v4
	v_add_u32_e32 v193, 0x10000, v5
	v_add_u32_e32 v194, 0x10400, v5
	v_add_u32_e32 v195, 0x10800, v5
	v_add_u32_e32 v196, 0x10c00, v5
	v_add_u32_e32 v197, 0x14000, v5
	v_add_u32_e32 v198, 0x14400, v5
	v_add_u32_e32 v199, 0x14800, v5
	v_add_u32_e32 v200, 0x14c00, v5
	v_add_u32_e32 v201, 0x18000, v5
	v_add_u32_e32 v202, 0x18400, v5
	v_add_u32_e32 v203, 0x18800, v5
	v_add_u32_e32 v204, 0x18c00, v5
	v_add_u32_e32 v205, 0x1c000, v5
	v_add_u32_e32 v206, 0x1c400, v5
	v_add_u32_e32 v207, 0x1c800, v5
	v_add_u32_e32 v208, 0x1cc00, v5
	v_add_u32_e32 v209, s1, v2
	s_mov_b32 s54, 0xc0c00000
	s_mov_b32 s12, 0xc01d265f
	s_mov_b32 s14, 0x3e800000
	v_mov_b32_e32 v210, 0x41000000
	s_mov_b32 s28, s0
	s_barrier
	s_branch .LBB0_498

.LBB0_506:
	ds_read_b128 v[52:55], v193
	ds_read_b128 v[66:69], v194
	ds_read_b128 v[70:73], v195
	ds_read_b128 v[74:77], v196
	ds_read_b128 v[78:81], v197
	ds_read_b128 v[176:179], v198
	ds_read_b128 v[180:183], v199
	ds_read_b128 v[212:215], v200
	s_add_u32 s30, s40, 0x80
	s_addc_u32 s31, s41, 0
	s_and_b64 s[18:19], s[18:19], exec
	s_cselect_b32 s31, s97, s31
	s_cselect_b32 s30, s96, s30
	s_cselect_b32 s19, s1, s57
	s_cselect_b32 s18, s21, s29
	v_lshl_add_u64 v[56:57], s[40:41], 0, v[42:43]
	s_add_i32 m0, s27, 0xc000
	ds_read_b128 v[220:223], v209
	ds_read_b128 v[224:227], v209 offset:1024
	ds_read_b128 v[228:231], v209 offset:2048
	ds_read_b128 v[232:235], v209 offset:3072
	ds_read_b128 v[236:239], v209 offset:4096
	ds_read_b128 v[240:243], v209 offset:5120
	ds_read_b128 v[244:247], v209 offset:6144
	ds_read_b128 v[248:251], v209 offset:7168
	global_load_lds_dwordx4 v[56:57], off
	v_lshl_add_u64 v[56:57], s[40:41], 0, v[44:45]
	s_add_i32 m0, s27, 0xe000
	s_nop 0
	global_load_lds_dwordx4 v[56:57], off
	s_cmp_lg_u32 s63, -2
	s_cbranch_scc1 .Lfw_p6a_s
	s_waitcnt vmcnt(10)
	s_branch .Lfw_p6a_d
.Lfw_p6a_s:
	s_waitcnt vmcnt(8)
.Lfw_p6a_d:
	s_waitcnt lgkmcnt(0)
	s_barrier
	s_setprio 1
	s_waitcnt lgkmcnt(0)
	v_mfma_i32_16x16x64_i8 v[158:161], v[52:55], v[220:223], v[158:161]
	v_mfma_i32_16x16x64_i8 v[150:153], v[70:73], v[220:223], v[150:153]
	v_mfma_i32_16x16x64_i8 v[142:145], v[52:55], v[228:231], v[142:145]
	v_mfma_i32_16x16x64_i8 v[134:137], v[70:73], v[228:231], v[134:137]
	v_mfma_i32_16x16x64_i8 v[126:129], v[52:55], v[236:239], v[126:129]
	v_mfma_i32_16x16x64_i8 v[118:121], v[70:73], v[236:239], v[118:121]
	v_mfma_i32_16x16x64_i8 v[110:113], v[52:55], v[244:247], v[110:113]
	v_mfma_i32_16x16x64_i8 v[102:105], v[70:73], v[244:247], v[102:105]
	v_mfma_i32_16x16x64_i8 v[158:161], v[66:69], v[224:227], v[158:161]
	v_mfma_i32_16x16x64_i8 v[150:153], v[74:77], v[224:227], v[150:153]
	v_mfma_i32_16x16x64_i8 v[142:145], v[66:69], v[232:235], v[142:145]
	v_mfma_i32_16x16x64_i8 v[134:137], v[74:77], v[232:235], v[134:137]
	v_mfma_i32_16x16x64_i8 v[126:129], v[66:69], v[240:243], v[126:129]
	v_mfma_i32_16x16x64_i8 v[118:121], v[74:77], v[240:243], v[118:121]
	v_mfma_i32_16x16x64_i8 v[110:113], v[66:69], v[248:251], v[110:113]
	v_mfma_i32_16x16x64_i8 v[102:105], v[74:77], v[248:251], v[102:105]
	s_setprio 0
	s_setprio 1
	v_mfma_i32_16x16x64_i8 v[154:157], v[78:81], v[220:223], v[154:157]
	v_mfma_i32_16x16x64_i8 v[146:149], v[180:183], v[220:223], v[146:149]
	v_mfma_i32_16x16x64_i8 v[138:141], v[78:81], v[228:231], v[138:141]
	v_mfma_i32_16x16x64_i8 v[130:133], v[180:183], v[228:231], v[130:133]
	v_mfma_i32_16x16x64_i8 v[122:125], v[78:81], v[236:239], v[122:125]
	v_mfma_i32_16x16x64_i8 v[114:117], v[180:183], v[236:239], v[114:117]
	v_mfma_i32_16x16x64_i8 v[106:109], v[78:81], v[244:247], v[106:109]
	v_mfma_i32_16x16x64_i8 v[98:101], v[180:183], v[244:247], v[98:101]
	v_mfma_i32_16x16x64_i8 v[154:157], v[176:179], v[224:227], v[154:157]
	v_mfma_i32_16x16x64_i8 v[146:149], v[212:215], v[224:227], v[146:149]
	v_mfma_i32_16x16x64_i8 v[138:141], v[176:179], v[232:235], v[138:141]
	v_mfma_i32_16x16x64_i8 v[130:133], v[212:215], v[232:235], v[130:133]
	v_mfma_i32_16x16x64_i8 v[122:125], v[176:179], v[240:243], v[122:125]
	v_mfma_i32_16x16x64_i8 v[114:117], v[212:215], v[240:243], v[114:117]
	v_mfma_i32_16x16x64_i8 v[106:109], v[176:179], v[248:251], v[106:109]
	v_mfma_i32_16x16x64_i8 v[98:101], v[212:215], v[248:251], v[98:101]
	s_setprio 0
	s_barrier
	s_mov_b32 m0, s35
	v_lshl_add_u64 v[172:173], s[18:19], 0, v[162:163]
	s_add_u32 s64, s18, 0x20000
	ds_read_b128 v[220:223], v209 offset:16384
	ds_read_b128 v[224:227], v209 offset:17408
	ds_read_b128 v[228:231], v209 offset:18432
	ds_read_b128 v[232:235], v209 offset:19456
	ds_read_b128 v[236:239], v209 offset:20480
	ds_read_b128 v[240:243], v209 offset:21504
	ds_read_b128 v[244:247], v209 offset:22528
	ds_read_b128 v[248:251], v209 offset:23552
	global_load_lds_dwordx4 v[172:173], off
	v_lshl_add_u64 v[184:185], s[18:19], 0, v[164:165]
	s_mov_b32 m0, s36
	s_addc_u32 s65, s19, 0
	global_load_lds_dwordx4 v[184:185], off
	v_lshl_add_u64 v[56:57], s[64:65], 0, v[162:163]
	s_mov_b32 m0, s37
	v_mov_b32_e32 v169, v167
	global_load_lds_dwordx4 v[56:57], off
	v_lshl_add_u64 v[56:57], s[64:65], 0, v[164:165]
	s_mov_b32 m0, s42
	v_lshl_add_u64 v[216:217], s[30:31], 0, v[166:167]
	global_load_lds_dwordx4 v[56:57], off
	s_mov_b32 m0, s27
	v_lshl_add_u64 v[218:219], s[30:31], 0, v[168:169]
	global_load_lds_dwordx4 v166, s[30:31]
	s_mov_b32 m0, s43
	s_nop 0
	global_load_lds_dwordx4 v168, s[30:31]
	s_cmp_lg_u32 s63, -2
	s_cbranch_scc1 .Lfw_p6b_s
	s_waitcnt vmcnt(16)
	s_branch .Lfw_p6b_d

.Lfw_p6b_d:
	s_waitcnt lgkmcnt(0)
	s_barrier
	s_setprio 1
	s_waitcnt lgkmcnt(0)
	v_mfma_i32_16x16x64_i8 v[94:97], v[52:55], v[220:223], v[94:97]
	v_mfma_i32_16x16x64_i8 v[86:89], v[70:73], v[220:223], v[86:89]
	v_mfma_i32_16x16x64_i8 v[62:65], v[52:55], v[228:231], v[62:65]
	v_mfma_i32_16x16x64_i8 v[38:41], v[70:73], v[228:231], v[38:41]
	v_mfma_i32_16x16x64_i8 v[26:29], v[52:55], v[236:239], v[26:29]
	v_mfma_i32_16x16x64_i8 v[18:21], v[70:73], v[236:239], v[18:21]
	v_mfma_i32_16x16x64_i8 v[10:13], v[52:55], v[244:247], v[10:13]
	v_mfma_i32_16x16x64_i8 v[2:5], v[70:73], v[244:247], v[2:5]
	v_mfma_i32_16x16x64_i8 v[94:97], v[66:69], v[224:227], v[94:97]
	v_mfma_i32_16x16x64_i8 v[86:89], v[74:77], v[224:227], v[86:89]
	v_mfma_i32_16x16x64_i8 v[62:65], v[66:69], v[232:235], v[62:65]
	v_mfma_i32_16x16x64_i8 v[38:41], v[74:77], v[232:235], v[38:41]
	v_mfma_i32_16x16x64_i8 v[26:29], v[66:69], v[240:243], v[26:29]
	v_mfma_i32_16x16x64_i8 v[18:21], v[74:77], v[240:243], v[18:21]
	v_mfma_i32_16x16x64_i8 v[10:13], v[66:69], v[248:251], v[10:13]
	v_mfma_i32_16x16x64_i8 v[2:5], v[74:77], v[248:251], v[2:5]
	s_setprio 0
	s_setprio 1
	v_mfma_i32_16x16x64_i8 v[56:59], v[78:81], v[228:231], v[58:61]
	v_mfma_i32_16x16x64_i8 v[22:25], v[180:183], v[228:231], v[22:25]
	v_mfma_i32_16x16x64_i8 v[34:37], v[78:81], v[236:239], v[34:37]
	v_mfma_i32_16x16x64_i8 v[30:33], v[180:183], v[236:239], v[30:33]
	v_mfma_i32_16x16x64_i8 v[14:17], v[78:81], v[244:247], v[14:17]
	v_mfma_i32_16x16x64_i8 v[6:9], v[180:183], v[244:247], v[6:9]
	v_mfma_i32_16x16x64_i8 v[52:55], v[78:81], v[220:223], v[90:93]
	v_mfma_i32_16x16x64_i8 v[66:69], v[180:183], v[220:223], v[82:85]
	v_mfma_i32_16x16x64_i8 v[56:59], v[176:179], v[232:235], v[56:59]
	v_mfma_i32_16x16x64_i8 v[22:25], v[212:215], v[232:235], v[22:25]
	v_mfma_i32_16x16x64_i8 v[34:37], v[176:179], v[240:243], v[34:37]
	v_mfma_i32_16x16x64_i8 v[30:33], v[212:215], v[240:243], v[30:33]
	v_mfma_i32_16x16x64_i8 v[14:17], v[176:179], v[248:251], v[14:17]
	v_mfma_i32_16x16x64_i8 v[6:9], v[212:215], v[248:251], v[6:9]
	v_mfma_i32_16x16x64_i8 v[52:55], v[176:179], v[224:227], v[52:55]
	v_mfma_i32_16x16x64_i8 v[66:69], v[212:215], v[224:227], v[66:69]
	s_setprio 0
	s_barrier
	ds_read_b128 v[70:73], v201
	ds_read_b128 v[74:77], v202
	ds_read_b128 v[78:81], v203
	ds_read_b128 v[82:85], v204
	ds_read_b128 v[176:179], v205
	ds_read_b128 v[180:183], v206
	ds_read_b128 v[212:215], v207
	ds_read_b128 v[220:223], v208
	s_mov_b32 m0, s44
	v_lshl_add_u64 v[48:49], s[30:31], 0, v[48:49]
	ds_read_b128 v[90:93], v209 offset:32768
	ds_read_b128 v[224:227], v209 offset:33792
	ds_read_b128 v[228:231], v209 offset:34816
	ds_read_b128 v[232:235], v209 offset:35840
	ds_read_b128 v[236:239], v209 offset:36864
	ds_read_b128 v[240:243], v209 offset:37888
	ds_read_b128 v[244:247], v209 offset:38912
	ds_read_b128 v[248:251], v209 offset:39936
	global_load_lds_dwordx4 v[48:49], off
	v_lshl_add_u64 v[46:47], s[30:31], 0, v[46:47]
	s_mov_b32 m0, s45
	s_nop 0
	global_load_lds_dwordx4 v[46:47], off
	s_waitcnt vmcnt(8)
	s_waitcnt lgkmcnt(0)
	s_barrier
	s_setprio 1
	s_waitcnt lgkmcnt(0)
	v_mfma_i32_16x16x64_i8 v[46:49], v[70:73], v[90:93], v[158:161]
	v_mfma_i32_16x16x64_i8 v[158:161], v[74:77], v[224:227], v[46:49]
	v_mfma_i32_16x16x64_i8 v[46:49], v[78:81], v[90:93], v[150:153]
	v_mfma_i32_16x16x64_i8 v[150:153], v[82:85], v[224:227], v[46:49]
	v_mfma_i32_16x16x64_i8 v[46:49], v[70:73], v[228:231], v[142:145]
	v_mfma_i32_16x16x64_i8 v[142:145], v[74:77], v[232:235], v[46:49]
	v_mfma_i32_16x16x64_i8 v[46:49], v[78:81], v[228:231], v[134:137]
	v_mfma_i32_16x16x64_i8 v[134:137], v[82:85], v[232:235], v[46:49]
	v_mfma_i32_16x16x64_i8 v[46:49], v[70:73], v[236:239], v[126:129]
	v_mfma_i32_16x16x64_i8 v[126:129], v[74:77], v[240:243], v[46:49]
	v_mfma_i32_16x16x64_i8 v[46:49], v[78:81], v[236:239], v[118:121]
	v_mfma_i32_16x16x64_i8 v[118:121], v[82:85], v[240:243], v[46:49]
	v_mfma_i32_16x16x64_i8 v[46:49], v[70:73], v[244:247], v[110:113]
	v_mfma_i32_16x16x64_i8 v[110:113], v[74:77], v[248:251], v[46:49]
	v_mfma_i32_16x16x64_i8 v[46:49], v[78:81], v[244:247], v[102:105]
	v_mfma_i32_16x16x64_i8 v[102:105], v[82:85], v[248:251], v[46:49]
	s_setprio 0
	s_setprio 1
	v_mfma_i32_16x16x64_i8 v[46:49], v[176:179], v[90:93], v[154:157]
	v_mfma_i32_16x16x64_i8 v[154:157], v[180:183], v[224:227], v[46:49]
	v_mfma_i32_16x16x64_i8 v[46:49], v[212:215], v[90:93], v[146:149]
	v_mfma_i32_16x16x64_i8 v[146:149], v[220:223], v[224:227], v[46:49]
	v_mfma_i32_16x16x64_i8 v[46:49], v[176:179], v[228:231], v[138:141]
	v_mfma_i32_16x16x64_i8 v[138:141], v[180:183], v[232:235], v[46:49]
	v_mfma_i32_16x16x64_i8 v[46:49], v[212:215], v[228:231], v[130:133]
	v_mfma_i32_16x16x64_i8 v[130:133], v[220:223], v[232:235], v[46:49]
	v_mfma_i32_16x16x64_i8 v[46:49], v[176:179], v[236:239], v[122:125]
	v_mfma_i32_16x16x64_i8 v[122:125], v[180:183], v[240:243], v[46:49]
	v_mfma_i32_16x16x64_i8 v[46:49], v[212:215], v[236:239], v[114:117]
	v_mfma_i32_16x16x64_i8 v[114:117], v[220:223], v[240:243], v[46:49]
	v_mfma_i32_16x16x64_i8 v[46:49], v[176:179], v[244:247], v[106:109]
	v_mfma_i32_16x16x64_i8 v[106:109], v[180:183], v[248:251], v[46:49]
	v_mfma_i32_16x16x64_i8 v[46:49], v[212:215], v[244:247], v[98:101]
	v_mfma_i32_16x16x64_i8 v[98:101], v[220:223], v[248:251], v[46:49]
	s_setprio 0
	s_barrier
	s_mov_b32 m0, s48
	v_lshl_add_u64 v[60:61], v[172:173], 0, s[6:7]
	s_add_u32 s18, s18, 0x20080
	s_nop 1
	ds_read_b128 v[46:49], v209 offset:49152
	ds_read_b128 v[224:227], v209 offset:50176
	ds_read_b128 v[228:231], v209 offset:51200
	ds_read_b128 v[232:235], v209 offset:52224
	ds_read_b128 v[236:239], v209 offset:53248
	ds_read_b128 v[240:243], v209 offset:54272
	ds_read_b128 v[244:247], v209 offset:55296
	ds_read_b128 v[248:251], v209 offset:56320
	global_load_lds_dwordx4 v[60:61], off
	v_lshl_add_u64 v[60:61], v[184:185], 0, s[6:7]
	s_mov_b32 m0, s49
	s_addc_u32 s19, s19, 0
	global_load_lds_dwordx4 v[60:61], off
	v_lshl_add_u64 v[60:61], s[18:19], 0, v[162:163]
	s_mov_b32 m0, s52
	s_nop 0
	global_load_lds_dwordx4 v[60:61], off
	v_lshl_add_u64 v[60:61], s[18:19], 0, v[164:165]
	s_mov_b32 m0, s53
	s_nop 0
	global_load_lds_dwordx4 v[60:61], off
	v_lshl_add_u64 v[60:61], v[216:217], 0, s[6:7]
	s_mov_b32 m0, s50
	s_nop 0
	global_load_lds_dwordx4 v[60:61], off
	v_lshl_add_u64 v[60:61], v[218:219], 0, s[6:7]
	s_mov_b32 m0, s51
	s_nop 0
	global_load_lds_dwordx4 v[60:61], off
	s_waitcnt vmcnt(8)
	s_waitcnt lgkmcnt(0)
	s_barrier
	s_setprio 1
	s_waitcnt lgkmcnt(0)
	v_mfma_i32_16x16x64_i8 v[90:93], v[70:73], v[46:49], v[94:97]
	v_mfma_i32_16x16x64_i8 v[86:89], v[78:81], v[46:49], v[86:89]
	v_mfma_i32_16x16x64_i8 v[60:63], v[70:73], v[228:231], v[62:65]
	v_mfma_i32_16x16x64_i8 v[38:41], v[78:81], v[228:231], v[38:41]
	v_mfma_i32_16x16x64_i8 v[26:29], v[70:73], v[236:239], v[26:29]
	v_mfma_i32_16x16x64_i8 v[18:21], v[78:81], v[236:239], v[18:21]
	v_mfma_i32_16x16x64_i8 v[10:13], v[70:73], v[244:247], v[10:13]
	v_mfma_i32_16x16x64_i8 v[2:5], v[78:81], v[244:247], v[2:5]
	v_mfma_i32_16x16x64_i8 v[94:97], v[74:77], v[224:227], v[90:93]
	v_mfma_i32_16x16x64_i8 v[86:89], v[82:85], v[224:227], v[86:89]
	v_mfma_i32_16x16x64_i8 v[62:65], v[74:77], v[232:235], v[60:63]
	v_mfma_i32_16x16x64_i8 v[38:41], v[82:85], v[232:235], v[38:41]
	v_mfma_i32_16x16x64_i8 v[26:29], v[74:77], v[240:243], v[26:29]
	v_mfma_i32_16x16x64_i8 v[18:21], v[82:85], v[240:243], v[18:21]
	v_mfma_i32_16x16x64_i8 v[10:13], v[74:77], v[248:251], v[10:13]
	v_mfma_i32_16x16x64_i8 v[2:5], v[82:85], v[248:251], v[2:5]
	s_setprio 0
	s_setprio 1
	v_mfma_i32_16x16x64_i8 v[52:55], v[176:179], v[46:49], v[52:55]
	v_mfma_i32_16x16x64_i8 v[46:49], v[212:215], v[46:49], v[66:69]
	v_mfma_i32_16x16x64_i8 v[82:85], v[220:223], v[224:227], v[46:49]
	v_mfma_i32_16x16x64_i8 v[46:49], v[176:179], v[228:231], v[56:59]
	v_mfma_i32_16x16x64_i8 v[22:25], v[212:215], v[228:231], v[22:25]
	v_mfma_i32_16x16x64_i8 v[34:37], v[176:179], v[236:239], v[34:37]
	v_mfma_i32_16x16x64_i8 v[30:33], v[212:215], v[236:239], v[30:33]
	v_mfma_i32_16x16x64_i8 v[14:17], v[176:179], v[244:247], v[14:17]
	v_mfma_i32_16x16x64_i8 v[6:9], v[212:215], v[244:247], v[6:9]
	v_mfma_i32_16x16x64_i8 v[90:93], v[180:183], v[224:227], v[52:55]
	v_mfma_i32_16x16x64_i8 v[58:61], v[180:183], v[232:235], v[46:49]
	v_mfma_i32_16x16x64_i8 v[22:25], v[220:223], v[232:235], v[22:25]
	v_mfma_i32_16x16x64_i8 v[34:37], v[180:183], v[240:243], v[34:37]
	v_mfma_i32_16x16x64_i8 v[30:33], v[220:223], v[240:243], v[30:33]
	v_mfma_i32_16x16x64_i8 v[14:17], v[180:183], v[248:251], v[14:17]
	v_mfma_i32_16x16x64_i8 v[6:9], v[220:223], v[248:251], v[6:9]
	s_setprio 0
	s_barrier
	s_add_i32 s63, s63, 2
	s_add_u32 s40, s40, 0x100
	s_addc_u32 s41, s41, 0
	s_add_u32 s29, s29, 0x100
	s_addc_u32 s57, s57, 0
	s_cmp_gt_u32 s63, 5
	s_cbranch_scc1 .LBB0_509

.LBB0_3067:
	s_lshl_b32 s6, s6, 5
	s_and_b32 s12, s6, 0x60
	s_lshl_b32 s1, s3, 13
	s_lshl_b32 s14, s12, 7
	s_add_u32 s45, s70, 0x645000
	s_addc_u32 s46, s71, 0
	v_readlane_b32 s48, v252, 0
	v_readlane_b32 s49, v252, 1
	v_readlane_b32 s50, v252, 2
	s_add_u32 s47, s48, 0x40000
	s_addc_u32 s48, s49, 0
	s_add_i32 s49, s25, 0x18000
	s_mov_b64 s[6:7], 0x80
	s_add_i32 s50, s25, 0x1a000
	v_readlane_b32 s51, v252, 3
	v_readlane_b32 s52, v252, 4
	v_lshl_add_u64 v[4:5], v[4:5], 0, s[6:7]
	s_mov_b32 m0, s49
	s_add_u32 s8, s70, 0x19200080
	s_waitcnt vmcnt(2)
	s_barrier
	global_load_lds_dwordx4 v[4:5], off
	v_lshl_add_u64 v[2:3], v[2:3], 0, s[6:7]
	s_mov_b32 m0, s50
	s_addc_u32 s9, s71, 0
	s_add_i32 s51, s25, 0x8000
	s_add_i32 s52, s25, 0xa000
	v_readlane_b32 s53, v252, 5
	global_load_lds_dwordx4 v[2:3], off
	v_lshl_add_u64 v[2:3], s[8:9], 0, v[166:167]
	s_mov_b32 m0, s51
	s_add_u32 s10, s28, 0x20080
	v_readlane_b32 s54, v252, 6
	global_load_lds_dwordx4 v[2:3], off
	v_lshl_add_u64 v[2:3], s[8:9], 0, v[168:169]
	s_mov_b32 m0, s52
	s_addc_u32 s11, s29, 0
	s_add_i32 s53, s25, 0x1c000
	global_load_lds_dwordx4 v[2:3], off
	v_lshl_add_u64 v[2:3], s[10:11], 0, v[162:163]
	s_mov_b32 m0, s53
	s_add_i32 s54, s25, 0x1e000
	global_load_lds_dwordx4 v[2:3], off
	v_lshl_add_u64 v[2:3], s[10:11], 0, v[164:165]
	s_mov_b32 m0, s54
	v_lshlrev_b32_e32 v5, 6, v0
	global_load_lds_dwordx4 v[2:3], off
	v_and_b32_e32 v2, 15, v0
	v_bfe_u32 v3, v0, 4, 2
	v_lshl_or_b32 v178, s3, 6, v2
	v_lshlrev_b32_e32 v4, 4, v3
	s_movk_i32 s3, 0x3c0
	v_lshlrev_b32_e32 v6, 2, v0
	v_lshl_or_b32 v2, v2, 6, v4
	v_and_or_b32 v5, v5, s3, v4
	v_and_b32_e32 v6, 32, v6
	s_waitcnt vmcnt(0)
	s_add_i32 s3, s14, 0
	v_readlane_b32 s55, v252, 7
	v_xad_u32 v5, v5, v6, s3
	v_xad_u32 v2, v2, v6, 0
	s_cmpk_lt_u32 s2, 0x100
	v_lshl_or_b32 v170, v3, 3, s12
	v_bfe_u32 v3, v0, 4, 1
	s_cselect_b64 s[10:11], -1, 0
	v_lshlrev_b32_e32 v179, 3, v3
	v_lshlrev_b32_e32 v180, 4, v3
	v_or_b32_e32 v181, 32, v4
	v_add_u32_e32 v182, 0x10000, v5
	v_add_u32_e32 v183, 0x10400, v5
	v_add_u32_e32 v184, 0x10800, v5
	v_add_u32_e32 v185, 0x10c00, v5
	v_add_u32_e32 v186, 0x14000, v5
	v_add_u32_e32 v187, 0x14400, v5
	v_add_u32_e32 v188, 0x14800, v5
	v_add_u32_e32 v189, 0x14c00, v5
	v_add_u32_e32 v190, 0x18000, v5
	v_add_u32_e32 v191, 0x18400, v5
	v_add_u32_e32 v192, 0x18800, v5
	v_add_u32_e32 v193, 0x18c00, v5
	v_add_u32_e32 v194, 0x1c000, v5
	v_add_u32_e32 v195, 0x1c400, v5
	v_add_u32_e32 v196, 0x1c800, v5
	v_add_u32_e32 v197, 0x1cc00, v5
	v_add_u32_e32 v198, s1, v2
	s_mov_b32 s55, 0xc0c00000
	s_mov_b32 s12, 0xc01d265f
	s_mov_b32 s14, 0x3e800000
	v_mov_b32_e32 v199, 0x41000000
	s_mov_b32 s26, s0
	s_barrier
	s_branch .LBB0_3070

.LBB0_3078:
	ds_read_b128 v[88:91], v182
	ds_read_b128 v[98:101], v183
	ds_read_b128 v[106:109], v184
	ds_read_b128 v[110:113], v185
	ds_read_b128 v[114:117], v186
	ds_read_b128 v[200:203], v187
	ds_read_b128 v[204:207], v188
	ds_read_b128 v[208:211], v189
	s_add_u32 s34, s28, 0x80
	s_addc_u32 s35, s29, 0
	s_and_b64 s[30:31], s[30:31], exec
	s_cselect_b32 s35, s97, s35
	s_cselect_b32 s34, s96, s34
	s_cselect_b32 s31, s1, s58
	s_cselect_b32 s30, s19, s27
	v_lshl_add_u64 v[92:93], s[28:29], 0, v[74:75]
	s_add_i32 m0, s25, 0xc000
	ds_read_b128 v[212:215], v198
	ds_read_b128 v[216:219], v198 offset:1024
	ds_read_b128 v[220:223], v198 offset:2048
	ds_read_b128 v[224:227], v198 offset:3072
	ds_read_b128 v[228:231], v198 offset:4096
	ds_read_b128 v[232:235], v198 offset:5120
	ds_read_b128 v[236:239], v198 offset:6144
	ds_read_b128 v[240:243], v198 offset:7168
	global_load_lds_dwordx4 v[92:93], off
	v_lshl_add_u64 v[92:93], s[28:29], 0, v[76:77]
	s_add_i32 m0, s25, 0xe000
	s_nop 0
	global_load_lds_dwordx4 v[92:93], off
	s_cmp_lg_u32 s59, -2
	s_cbranch_scc1 .Lfw_p16a_s
	s_waitcnt vmcnt(10)
	s_branch .Lfw_p16a_d

.Lfw_p16a_d:
	s_waitcnt lgkmcnt(0)
	s_barrier
	s_setprio 1
	s_waitcnt lgkmcnt(0)
	v_mfma_i32_16x16x64_i8 v[158:161], v[88:91], v[212:215], v[158:161]
	v_mfma_i32_16x16x64_i8 v[150:153], v[106:109], v[212:215], v[150:153]
	v_mfma_i32_16x16x64_i8 v[142:145], v[88:91], v[220:223], v[142:145]
	v_mfma_i32_16x16x64_i8 v[134:137], v[106:109], v[220:223], v[134:137]
	v_mfma_i32_16x16x64_i8 v[126:129], v[88:91], v[228:231], v[126:129]
	v_mfma_i32_16x16x64_i8 v[118:121], v[106:109], v[228:231], v[118:121]
	v_mfma_i32_16x16x64_i8 v[92:95], v[88:91], v[236:239], v[94:97]
	v_mfma_i32_16x16x64_i8 v[70:73], v[106:109], v[236:239], v[70:73]
	v_mfma_i32_16x16x64_i8 v[158:161], v[98:101], v[216:219], v[158:161]
	v_mfma_i32_16x16x64_i8 v[150:153], v[110:113], v[216:219], v[150:153]
	v_mfma_i32_16x16x64_i8 v[142:145], v[98:101], v[224:227], v[142:145]
	v_mfma_i32_16x16x64_i8 v[134:137], v[110:113], v[224:227], v[134:137]
	v_mfma_i32_16x16x64_i8 v[126:129], v[98:101], v[232:235], v[126:129]
	v_mfma_i32_16x16x64_i8 v[118:121], v[110:113], v[232:235], v[118:121]
	v_mfma_i32_16x16x64_i8 v[92:95], v[98:101], v[240:243], v[92:95]
	v_mfma_i32_16x16x64_i8 v[70:73], v[110:113], v[240:243], v[70:73]
	s_setprio 0
	s_setprio 1
	v_mfma_i32_16x16x64_i8 v[154:157], v[114:117], v[212:215], v[154:157]
	v_mfma_i32_16x16x64_i8 v[146:149], v[204:207], v[212:215], v[146:149]
	v_mfma_i32_16x16x64_i8 v[138:141], v[114:117], v[220:223], v[138:141]
	v_mfma_i32_16x16x64_i8 v[130:133], v[204:207], v[220:223], v[130:133]
	v_mfma_i32_16x16x64_i8 v[122:125], v[114:117], v[228:231], v[122:125]
	v_mfma_i32_16x16x64_i8 v[102:105], v[204:207], v[228:231], v[102:105]
	v_mfma_i32_16x16x64_i8 v[78:81], v[114:117], v[236:239], v[78:81]
	v_mfma_i32_16x16x64_i8 v[66:69], v[204:207], v[236:239], v[66:69]
	v_mfma_i32_16x16x64_i8 v[154:157], v[200:203], v[216:219], v[154:157]
	v_mfma_i32_16x16x64_i8 v[146:149], v[208:211], v[216:219], v[146:149]
	v_mfma_i32_16x16x64_i8 v[138:141], v[200:203], v[224:227], v[138:141]
	v_mfma_i32_16x16x64_i8 v[130:133], v[208:211], v[224:227], v[130:133]
	v_mfma_i32_16x16x64_i8 v[122:125], v[200:203], v[232:235], v[122:125]
	v_mfma_i32_16x16x64_i8 v[102:105], v[208:211], v[232:235], v[102:105]
	v_mfma_i32_16x16x64_i8 v[78:81], v[200:203], v[240:243], v[78:81]
	v_mfma_i32_16x16x64_i8 v[66:69], v[208:211], v[240:243], v[66:69]
	s_setprio 0
	s_barrier
	s_mov_b32 m0, s38
	v_lshl_add_u64 v[172:173], s[30:31], 0, v[162:163]
	s_add_u32 s60, s30, 0x20000
	ds_read_b128 v[212:215], v198 offset:16384
	ds_read_b128 v[216:219], v198 offset:17408
	ds_read_b128 v[220:223], v198 offset:18432
	ds_read_b128 v[224:227], v198 offset:19456
	ds_read_b128 v[228:231], v198 offset:20480
	ds_read_b128 v[232:235], v198 offset:21504
	ds_read_b128 v[236:239], v198 offset:22528
	ds_read_b128 v[240:243], v198 offset:23552
	global_load_lds_dwordx4 v[172:173], off
	v_lshl_add_u64 v[244:245], s[30:31], 0, v[164:165]
	s_mov_b32 m0, s39
	s_addc_u32 s61, s31, 0
	global_load_lds_dwordx4 v[244:245], off
	v_lshl_add_u64 v[96:97], s[60:61], 0, v[162:163]
	s_mov_b32 m0, s40
	v_mov_b32_e32 v169, v167
	global_load_lds_dwordx4 v[96:97], off
	v_lshl_add_u64 v[96:97], s[60:61], 0, v[164:165]
	s_mov_b32 m0, s41
	v_lshl_add_u64 v[246:247], s[34:35], 0, v[166:167]
	global_load_lds_dwordx4 v[96:97], off
	s_mov_b32 m0, s25
	v_lshl_add_u64 v[248:249], s[34:35], 0, v[168:169]
	global_load_lds_dwordx4 v166, s[34:35]
	s_mov_b32 m0, s42
	s_nop 0
	global_load_lds_dwordx4 v168, s[34:35]
	s_cmp_lg_u32 s59, -2
	s_cbranch_scc1 .Lfw_p16b_s
	s_waitcnt vmcnt(16)
	s_branch .Lfw_p16b_d

.Lfw_p16b_d:
	s_waitcnt lgkmcnt(0)
	s_barrier
	s_setprio 1
	s_waitcnt lgkmcnt(0)
	v_mfma_i32_16x16x64_i8 v[62:65], v[88:91], v[212:215], v[62:65]
	v_mfma_i32_16x16x64_i8 v[54:57], v[106:109], v[212:215], v[54:57]
	v_mfma_i32_16x16x64_i8 v[46:49], v[88:91], v[220:223], v[46:49]
	v_mfma_i32_16x16x64_i8 v[38:41], v[106:109], v[220:223], v[38:41]
	v_mfma_i32_16x16x64_i8 v[22:25], v[88:91], v[228:231], v[22:25]
	v_mfma_i32_16x16x64_i8 v[14:17], v[106:109], v[228:231], v[14:17]
	v_mfma_i32_16x16x64_i8 v[6:9], v[88:91], v[236:239], v[6:9]
	v_mfma_i32_16x16x64_i8 v[2:5], v[106:109], v[236:239], v[2:5]
	v_mfma_i32_16x16x64_i8 v[62:65], v[98:101], v[216:219], v[62:65]
	v_mfma_i32_16x16x64_i8 v[54:57], v[110:113], v[216:219], v[54:57]
	v_mfma_i32_16x16x64_i8 v[46:49], v[98:101], v[224:227], v[46:49]
	v_mfma_i32_16x16x64_i8 v[38:41], v[110:113], v[224:227], v[38:41]
	v_mfma_i32_16x16x64_i8 v[22:25], v[98:101], v[232:235], v[22:25]
	v_mfma_i32_16x16x64_i8 v[14:17], v[110:113], v[232:235], v[14:17]
	v_mfma_i32_16x16x64_i8 v[6:9], v[98:101], v[240:243], v[6:9]
	v_mfma_i32_16x16x64_i8 v[2:5], v[110:113], v[240:243], v[2:5]
	s_setprio 0
	s_setprio 1
	v_mfma_i32_16x16x64_i8 v[58:61], v[114:117], v[212:215], v[58:61]
	v_mfma_i32_16x16x64_i8 v[50:53], v[204:207], v[212:215], v[50:53]
	v_mfma_i32_16x16x64_i8 v[42:45], v[114:117], v[220:223], v[42:45]
	v_mfma_i32_16x16x64_i8 v[30:33], v[204:207], v[220:223], v[30:33]
	v_mfma_i32_16x16x64_i8 v[34:37], v[114:117], v[228:231], v[34:37]
	v_mfma_i32_16x16x64_i8 v[26:29], v[204:207], v[228:231], v[26:29]
	v_mfma_i32_16x16x64_i8 v[18:21], v[114:117], v[236:239], v[18:21]
	v_mfma_i32_16x16x64_i8 v[10:13], v[204:207], v[236:239], v[10:13]
	v_mfma_i32_16x16x64_i8 v[58:61], v[200:203], v[216:219], v[58:61]
	v_mfma_i32_16x16x64_i8 v[50:53], v[208:211], v[216:219], v[50:53]
	v_mfma_i32_16x16x64_i8 v[42:45], v[200:203], v[224:227], v[42:45]
	v_mfma_i32_16x16x64_i8 v[30:33], v[208:211], v[224:227], v[30:33]
	v_mfma_i32_16x16x64_i8 v[34:37], v[200:203], v[232:235], v[34:37]
	v_mfma_i32_16x16x64_i8 v[26:29], v[208:211], v[232:235], v[26:29]
	v_mfma_i32_16x16x64_i8 v[18:21], v[200:203], v[240:243], v[18:21]
	v_mfma_i32_16x16x64_i8 v[10:13], v[208:211], v[240:243], v[10:13]
	s_setprio 0
	s_barrier
	ds_read_b128 v[88:91], v190
	ds_read_b128 v[98:101], v191
	ds_read_b128 v[106:109], v192
	ds_read_b128 v[110:113], v193
	ds_read_b128 v[114:117], v194
	ds_read_b128 v[200:203], v195
	ds_read_b128 v[204:207], v196
	ds_read_b128 v[208:211], v197
	s_mov_b32 m0, s43
	v_lshl_add_u64 v[84:85], s[34:35], 0, v[84:85]
	ds_read_b128 v[212:215], v198 offset:32768
	ds_read_b128 v[216:219], v198 offset:33792
	ds_read_b128 v[220:223], v198 offset:34816
	ds_read_b128 v[224:227], v198 offset:35840
	ds_read_b128 v[228:231], v198 offset:36864
	ds_read_b128 v[232:235], v198 offset:37888
	ds_read_b128 v[236:239], v198 offset:38912
	ds_read_b128 v[240:243], v198 offset:39936
	global_load_lds_dwordx4 v[84:85], off
	v_lshl_add_u64 v[82:83], s[34:35], 0, v[82:83]
	s_mov_b32 m0, s44
	s_nop 0
	global_load_lds_dwordx4 v[82:83], off
	s_waitcnt vmcnt(8)
	s_waitcnt lgkmcnt(0)
	s_barrier
	s_setprio 1
	s_waitcnt lgkmcnt(0)
	v_mfma_i32_16x16x64_i8 v[82:85], v[88:91], v[212:215], v[158:161]
	v_mfma_i32_16x16x64_i8 v[158:161], v[98:101], v[216:219], v[82:85]
	v_mfma_i32_16x16x64_i8 v[82:85], v[106:109], v[212:215], v[150:153]
	v_mfma_i32_16x16x64_i8 v[150:153], v[110:113], v[216:219], v[82:85]
	v_mfma_i32_16x16x64_i8 v[82:85], v[88:91], v[220:223], v[142:145]
	v_mfma_i32_16x16x64_i8 v[142:145], v[98:101], v[224:227], v[82:85]
	v_mfma_i32_16x16x64_i8 v[82:85], v[106:109], v[220:223], v[134:137]
	v_mfma_i32_16x16x64_i8 v[134:137], v[110:113], v[224:227], v[82:85]
	v_mfma_i32_16x16x64_i8 v[82:85], v[88:91], v[228:231], v[126:129]
	v_mfma_i32_16x16x64_i8 v[126:129], v[98:101], v[232:235], v[82:85]
	v_mfma_i32_16x16x64_i8 v[82:85], v[106:109], v[228:231], v[118:121]
	v_mfma_i32_16x16x64_i8 v[118:121], v[110:113], v[232:235], v[82:85]
	v_mfma_i32_16x16x64_i8 v[82:85], v[88:91], v[236:239], v[92:95]
	v_mfma_i32_16x16x64_i8 v[70:73], v[106:109], v[236:239], v[70:73]
	v_mfma_i32_16x16x64_i8 v[94:97], v[98:101], v[240:243], v[82:85]
	v_mfma_i32_16x16x64_i8 v[70:73], v[110:113], v[240:243], v[70:73]
	s_setprio 0
	s_setprio 1
	v_mfma_i32_16x16x64_i8 v[82:85], v[114:117], v[212:215], v[154:157]
	v_mfma_i32_16x16x64_i8 v[154:157], v[200:203], v[216:219], v[82:85]
	v_mfma_i32_16x16x64_i8 v[82:85], v[204:207], v[212:215], v[146:149]
	v_mfma_i32_16x16x64_i8 v[146:149], v[208:211], v[216:219], v[82:85]
	v_mfma_i32_16x16x64_i8 v[82:85], v[114:117], v[220:223], v[138:141]
	v_mfma_i32_16x16x64_i8 v[138:141], v[200:203], v[224:227], v[82:85]
	v_mfma_i32_16x16x64_i8 v[82:85], v[204:207], v[220:223], v[130:133]
	v_mfma_i32_16x16x64_i8 v[130:133], v[208:211], v[224:227], v[82:85]
	v_mfma_i32_16x16x64_i8 v[82:85], v[114:117], v[228:231], v[122:125]
	v_mfma_i32_16x16x64_i8 v[122:125], v[200:203], v[232:235], v[82:85]
	v_mfma_i32_16x16x64_i8 v[82:85], v[204:207], v[228:231], v[102:105]
	v_mfma_i32_16x16x64_i8 v[78:81], v[114:117], v[236:239], v[78:81]
	v_mfma_i32_16x16x64_i8 v[66:69], v[204:207], v[236:239], v[66:69]
	v_mfma_i32_16x16x64_i8 v[102:105], v[208:211], v[232:235], v[82:85]
	v_mfma_i32_16x16x64_i8 v[78:81], v[200:203], v[240:243], v[78:81]
	v_mfma_i32_16x16x64_i8 v[66:69], v[208:211], v[240:243], v[66:69]
	s_setprio 0
	s_barrier
	s_mov_b32 m0, s49
	v_lshl_add_u64 v[92:93], v[172:173], 0, s[6:7]
	s_add_u32 s30, s30, 0x20080
	ds_read_b128 v[82:85], v198 offset:49152
	ds_read_b128 v[212:215], v198 offset:50176
	ds_read_b128 v[216:219], v198 offset:51200
	ds_read_b128 v[220:223], v198 offset:52224
	ds_read_b128 v[224:227], v198 offset:53248
	ds_read_b128 v[228:231], v198 offset:54272
	ds_read_b128 v[232:235], v198 offset:55296
	ds_read_b128 v[236:239], v198 offset:56320
	global_load_lds_dwordx4 v[92:93], off
	v_lshl_add_u64 v[92:93], v[244:245], 0, s[6:7]
	s_mov_b32 m0, s50
	s_addc_u32 s31, s31, 0
	global_load_lds_dwordx4 v[92:93], off
	v_lshl_add_u64 v[92:93], s[30:31], 0, v[162:163]
	s_mov_b32 m0, s53
	s_nop 0
	global_load_lds_dwordx4 v[92:93], off
	v_lshl_add_u64 v[92:93], s[30:31], 0, v[164:165]
	s_mov_b32 m0, s54
	s_nop 0
	global_load_lds_dwordx4 v[92:93], off
	v_lshl_add_u64 v[92:93], v[246:247], 0, s[6:7]
	s_mov_b32 m0, s51
	s_nop 0
	global_load_lds_dwordx4 v[92:93], off
	v_lshl_add_u64 v[92:93], v[248:249], 0, s[6:7]
	s_mov_b32 m0, s52
	s_nop 0
	global_load_lds_dwordx4 v[92:93], off
	s_waitcnt vmcnt(8)
	s_waitcnt lgkmcnt(0)
	s_barrier
	s_setprio 1
	s_waitcnt lgkmcnt(0)
	v_mfma_i32_16x16x64_i8 v[62:65], v[88:91], v[82:85], v[62:65]
	v_mfma_i32_16x16x64_i8 v[54:57], v[106:109], v[82:85], v[54:57]
	v_mfma_i32_16x16x64_i8 v[46:49], v[88:91], v[216:219], v[46:49]
	v_mfma_i32_16x16x64_i8 v[38:41], v[106:109], v[216:219], v[38:41]
	v_mfma_i32_16x16x64_i8 v[22:25], v[88:91], v[224:227], v[22:25]
	v_mfma_i32_16x16x64_i8 v[14:17], v[106:109], v[224:227], v[14:17]
	v_mfma_i32_16x16x64_i8 v[6:9], v[88:91], v[232:235], v[6:9]
	v_mfma_i32_16x16x64_i8 v[2:5], v[106:109], v[232:235], v[2:5]
	v_mfma_i32_16x16x64_i8 v[62:65], v[98:101], v[212:215], v[62:65]
	v_mfma_i32_16x16x64_i8 v[54:57], v[110:113], v[212:215], v[54:57]
	v_mfma_i32_16x16x64_i8 v[46:49], v[98:101], v[220:223], v[46:49]
	v_mfma_i32_16x16x64_i8 v[38:41], v[110:113], v[220:223], v[38:41]
	v_mfma_i32_16x16x64_i8 v[22:25], v[98:101], v[228:231], v[22:25]
	v_mfma_i32_16x16x64_i8 v[14:17], v[110:113], v[228:231], v[14:17]
	v_mfma_i32_16x16x64_i8 v[6:9], v[98:101], v[236:239], v[6:9]
	v_mfma_i32_16x16x64_i8 v[2:5], v[110:113], v[236:239], v[2:5]
	s_setprio 0
	s_setprio 1
	v_mfma_i32_16x16x64_i8 v[58:61], v[114:117], v[82:85], v[58:61]
	v_mfma_i32_16x16x64_i8 v[50:53], v[204:207], v[82:85], v[50:53]
	v_mfma_i32_16x16x64_i8 v[42:45], v[114:117], v[216:219], v[42:45]
	v_mfma_i32_16x16x64_i8 v[30:33], v[204:207], v[216:219], v[30:33]
	v_mfma_i32_16x16x64_i8 v[34:37], v[114:117], v[224:227], v[34:37]
	v_mfma_i32_16x16x64_i8 v[26:29], v[204:207], v[224:227], v[26:29]
	v_mfma_i32_16x16x64_i8 v[18:21], v[114:117], v[232:235], v[18:21]
	v_mfma_i32_16x16x64_i8 v[10:13], v[204:207], v[232:235], v[10:13]
	v_mfma_i32_16x16x64_i8 v[58:61], v[200:203], v[212:215], v[58:61]
	v_mfma_i32_16x16x64_i8 v[50:53], v[208:211], v[212:215], v[50:53]
	v_mfma_i32_16x16x64_i8 v[42:45], v[200:203], v[220:223], v[42:45]
	v_mfma_i32_16x16x64_i8 v[30:33], v[208:211], v[220:223], v[30:33]
	v_mfma_i32_16x16x64_i8 v[34:37], v[200:203], v[228:231], v[34:37]
	v_mfma_i32_16x16x64_i8 v[26:29], v[208:211], v[228:231], v[26:29]
	v_mfma_i32_16x16x64_i8 v[18:21], v[200:203], v[236:239], v[18:21]
	v_mfma_i32_16x16x64_i8 v[10:13], v[208:211], v[236:239], v[10:13]
	s_setprio 0
	s_barrier
	s_add_i32 s59, s59, 2
	s_add_u32 s28, s28, 0x100
	s_addc_u32 s29, s29, 0
	s_add_u32 s27, s27, 0x100
	s_addc_u32 s58, s58, 0
	s_cmp_gt_u32 s59, 5
	s_cbranch_scc1 .LBB0_3081
